# stick-breaking tile loop: dropped the redundant in-loop vmcnt waits (Q fragments are drained at unit start) that stalled on the just-issued LDS-DMA pieces
# speedup vs baseline: 1.0192x; 1.0071x over previous
; #define LAS __attribute__((address_space(3)))
; __device__ __forceinline__ int crow(int r, int hi) { return (r & 3) + 8 * (r >> 2) + 4 * hi; }
; template <bool diag> __device__ __forceinline__ void sb_tile_math_t(f32x16& z0, f32x16& z1, float& carry, int s0, int tq, int hi) {
;         f32x16 q0, q1;
; #pragma unroll
;         for (int r = 0; r < 16; ++r) {
;             const int kv = s0 + crow(r, hi);
;             { float q = __builtin_amdgcn_rcpf(1.0f + __builtin_amdgcn_exp2f(z0[r])); if (diag && !(kv < tq)) q = 1.f; q0[r] = q; }
;             { float q = __builtin_amdgcn_rcpf(1.0f + __builtin_amdgcn_exp2f(z1[r])); if (diag && !(kv + 32 < tq)) q = 1.f; q1[r] = q; }
;         }
;         float own[8], oth[8], S[8];
; #pragma unroll
;         for (int G = 0; G < 4; ++G) { own[G] = (q0[4 * G] * q0[4 * G + 1]) * (q0[4 * G + 2] * q0[4 * G + 3]); own[4 + G] = (q1[4 * G] * q1[4 * G + 1]) * (q1[4 * G + 2] * q1[4 * G + 3]); }
; #pragma unroll
;         for (int i = 0; i < 8; ++i) { const auto rr = __builtin_amdgcn_permlane32_swap(__float_as_uint(own[i]), __float_as_uint(own[i]), false, false);
;             own[i] = __uint_as_float(rr[0]) * __uint_as_float(rr[1]); oth[i] = __uint_as_float(rr[1]); }
; __device__ __forceinline__ void sb_block_unit(bf16x8 (&qr)[4], int b, int hp  , int u  , int nb, int nhp, int nu, const bf16_t* Q, const bf16_t* K, const bf16_t* V, bf16_t* O, LAS char* L, int wid, int lane) {
;     ...
;         if (j <= jdw && !gone) {
;             bf16x8 kf[8];
; #pragma unroll
;             for (int d0 = 0; d0 < 4; ++d0) { kf[2 * d0] = *(const LAS bf16x8*)(kp0 + sc + d0 * 2048); kf[2 * d0 + 1] = *(const LAS bf16x8*)(kp0 + sc + d0 * 2048 + 512); }
;             __builtin_amdgcn_sched_barrier(0);
;             f32x16 z0, z1; qkt(z0, z1, kf, qr);
;             bf16x8 vf[8]; pv_load(vf, vp0 + sc);
;             __builtin_amdgcn_sched_barrier(0);
;             sb_tile_math(z0, z1, carry, j == jdw, j * 64, tq, hi);
;             pv_mma(o, vf, z0, z1);
.LBB0_358:
	s_cmp_le_i32 s33, s97
	s_cselect_b64 s[88:89], -1, 0
	s_xor_b64 s[94:95], s[4:5], -1
	s_and_b64 s[88:89], s[88:89], s[94:95]
	s_and_saveexec_b64 s[94:95], s[88:89]
	s_cbranch_execz .LBB0_370
	v_add_u32_e32 v38, s1, v146
	ds_read_b128 v[34:37], v38
	ds_read_b128 v[50:53], v38 offset:512
	ds_read_b128 v[82:85], v38 offset:2048
	ds_read_b128 v[86:89], v38 offset:2560
	ds_read_b128 v[90:93], v38 offset:4096
	ds_read_b128 v[94:97], v38 offset:4608
	ds_read_b128 v[98:101], v38 offset:6144
	ds_read_b128 v[102:105], v38 offset:6656
	s_waitcnt lgkmcnt(7)
	v_mfma_f32_32x32x16_bf16 v[34:49], v[34:37], v[66:69], 0
	s_waitcnt lgkmcnt(6)
	v_mfma_f32_32x32x16_bf16 v[50:65], v[50:53], v[66:69], 0
	s_waitcnt lgkmcnt(5)
	v_mfma_f32_32x32x16_bf16 v[34:49], v[82:85], v[70:73], v[34:49]
	s_waitcnt lgkmcnt(4)
	v_mfma_f32_32x32x16_bf16 v[50:65], v[86:89], v[70:73], v[50:65]
	s_waitcnt lgkmcnt(3)
	v_mfma_f32_32x32x16_bf16 v[34:49], v[90:93], v[74:77], v[34:49]
	v_add_u32_e32 v92, s1, v147
	s_waitcnt lgkmcnt(2)
	v_mfma_f32_32x32x16_bf16 v[50:65], v[94:97], v[74:77], v[50:65]
	s_waitcnt lgkmcnt(1)
	v_mfma_f32_32x32x16_bf16 v[34:49], v[98:101], v[78:81], v[34:49]
	s_waitcnt lgkmcnt(0)
	v_mfma_f32_32x32x16_bf16 v[50:65], v[102:105], v[78:81], v[50:65]
	ds_read_b64_tr_b16 v[110:111], v92 offset:8192
	ds_read_b64_tr_b16 v[112:113], v92 offset:8704
	ds_read_b64_tr_b16 v[106:107], v92 offset:12288
	ds_read_b64_tr_b16 v[108:109], v92 offset:12800
	ds_read_b64_tr_b16 v[102:103], v92 offset:9216
	ds_read_b64_tr_b16 v[104:105], v92 offset:9728
	ds_read_b64_tr_b16 v[98:99], v92 offset:13312
	ds_read_b64_tr_b16 v[100:101], v92 offset:13824
	ds_read_b64_tr_b16 v[94:95], v92 offset:10240
	ds_read_b64_tr_b16 v[96:97], v92 offset:10752
	ds_read_b64_tr_b16 v[86:87], v92 offset:14336
	ds_read_b64_tr_b16 v[88:89], v92 offset:14848
	ds_read_b64_tr_b16 v[82:83], v92 offset:11264
	ds_read_b64_tr_b16 v[84:85], v92 offset:11776
	ds_read_b64_tr_b16 v[90:91], v92 offset:15360
	ds_read_b64_tr_b16 v[92:93], v92 offset:15872
	v_exp_f32_e32 v34, v34
	v_exp_f32_e32 v179, v50
	v_exp_f32_e32 v177, v35
	v_exp_f32_e32 v175, v51
	v_add_f32_e32 v34, 1.0, v34
	v_rcp_f32_e32 v34, v34
	v_exp_f32_e32 v178, v36
	v_exp_f32_e32 v176, v52
	v_exp_f32_e32 v174, v37
	v_exp_f32_e32 v173, v53
	v_exp_f32_e32 v172, v38
	v_exp_f32_e32 v171, v54
	v_exp_f32_e32 v170, v39
	v_exp_f32_e32 v169, v55
	v_exp_f32_e32 v168, v40
	v_exp_f32_e32 v167, v56
	v_exp_f32_e32 v166, v41
	v_exp_f32_e32 v165, v57
	v_exp_f32_e32 v164, v42
	v_exp_f32_e32 v163, v58
	v_exp_f32_e32 v162, v43
	v_exp_f32_e32 v161, v59
	v_exp_f32_e32 v160, v44
	v_exp_f32_e32 v159, v60
	v_exp_f32_e32 v158, v45
	v_exp_f32_e32 v157, v61
	v_exp_f32_e32 v156, v46
	v_exp_f32_e32 v155, v62
	v_exp_f32_e32 v154, v47
	v_exp_f32_e32 v125, v63
	v_exp_f32_e32 v123, v48
	v_exp_f32_e32 v121, v64
	v_exp_f32_e32 v119, v49
	v_exp_f32_e32 v117, v65
	s_cmp_lg_u32 s96, s33
	s_mov_b64 vcc, -1
	s_cbranch_scc0 .LBB0_361
	v_add_f32_e32 v36, 1.0, v176
	v_rcp_f32_e32 v53, v36
	v_add_f32_e32 v36, 1.0, v174
	v_rcp_f32_e32 v47, v36
	v_add_f32_e32 v36, 1.0, v173
	v_rcp_f32_e32 v55, v36
	v_add_f32_e32 v36, 1.0, v172
	v_rcp_f32_e32 v56, v36
	v_add_f32_e32 v36, 1.0, v171
	v_rcp_f32_e32 v38, v36
	v_add_f32_e32 v36, 1.0, v170
	v_add_f32_e32 v35, 1.0, v179
	v_rcp_f32_e32 v58, v36
	v_add_f32_e32 v36, 1.0, v169
	v_rcp_f32_e32 v52, v35
	v_add_f32_e32 v35, 1.0, v177
	v_rcp_f32_e32 v44, v36
	v_add_f32_e32 v36, 1.0, v168
	v_rcp_f32_e32 v46, v35
	v_add_f32_e32 v35, 1.0, v175
	v_rcp_f32_e32 v57, v36
	v_add_f32_e32 v36, 1.0, v167
	v_rcp_f32_e32 v54, v35
	v_rcp_f32_e32 v39, v36
	v_add_f32_e32 v36, 1.0, v166
	v_add_f32_e32 v37, 1.0, v162
	v_rcp_f32_e32 v59, v36
	v_add_f32_e32 v36, 1.0, v165
	v_rcp_f32_e32 v64, v37
	v_add_f32_e32 v37, 1.0, v161
	v_rcp_f32_e32 v45, v36
	v_add_f32_e32 v36, 1.0, v164
	v_rcp_f32_e32 v42, v37
	v_add_f32_e32 v37, 1.0, v160
	v_add_f32_e32 v40, 1.0, v158
	v_add_f32_e32 v41, 1.0, v154
	v_rcp_f32_e32 v60, v36
	v_add_f32_e32 v36, 1.0, v163
	v_rcp_f32_e32 v61, v37
	v_add_f32_e32 v37, 1.0, v159
	v_rcp_f32_e32 v65, v40
	v_add_f32_e32 v40, 1.0, v157
	v_rcp_f32_e32 v132, v41
	v_add_f32_e32 v41, 1.0, v125
	v_rcp_f32_e32 v36, v36
	v_rcp_f32_e32 v37, v37
	v_rcp_f32_e32 v43, v40
	v_add_f32_e32 v40, 1.0, v156
	v_rcp_f32_e32 v48, v41
	v_add_f32_e32 v41, 1.0, v123
	v_add_f32_e32 v49, 1.0, v119
	v_pk_mul_f32 v[62:63], v[52:53], v[54:55]
	v_rcp_f32_e32 v128, v40
	v_rcp_f32_e32 v129, v41
	v_rcp_f32_e32 v133, v49
	v_pk_mul_f32 v[126:127], v[62:63], v[62:63] op_sel:[0,1] op_sel_hi:[1,0]
	v_pk_mul_f32 v[62:63], v[56:57], v[58:59]
	v_add_f32_e32 v35, 1.0, v178
	v_pk_mul_f32 v[130:131], v[62:63], v[62:63] op_sel:[0,1] op_sel_hi:[1,0]
	v_pk_mul_f32 v[62:63], v[38:39], v[44:45]
	v_add_f32_e32 v40, 1.0, v155
	v_pk_mul_f32 v[140:141], v[62:63], v[62:63] op_sel:[0,1] op_sel_hi:[1,0]
	v_pk_mul_f32 v[62:63], v[60:61], v[64:65]
	v_add_f32_e32 v41, 1.0, v121
	v_pk_mul_f32 v[134:135], v[62:63], v[62:63] op_sel:[0,1] op_sel_hi:[1,0]
	v_pk_mul_f32 v[62:63], v[36:37], v[42:43]
	v_add_f32_e32 v49, 1.0, v117
	v_pk_mul_f32 v[180:181], v[62:63], v[62:63] op_sel:[0,1] op_sel_hi:[1,0]
	v_pk_mul_f32 v[62:63], v[128:129], v[132:133]
	v_rcp_f32_e32 v35, v35
	v_rcp_f32_e32 v40, v40
	v_rcp_f32_e32 v41, v41
	v_rcp_f32_e32 v49, v49
	v_pk_mul_f32 v[138:139], v[62:63], v[62:63] op_sel:[0,1] op_sel_hi:[1,0]
	v_mov_b32_e32 v137, v134
	s_nop 1
	v_permlane32_swap_b32_e32 v134, v137
	v_mov_b32_e32 v135, v138
	v_mov_b32_e32 v131, v134
	s_nop 0
	v_permlane32_swap_b32_e32 v138, v135
	v_mov_b32_e32 v134, v126
	s_nop 1
	v_permlane32_swap_b32_e32 v126, v134
	v_mov_b32_e32 v127, v138
	v_pk_mul_f32 v[50:51], v[34:35], v[46:47]
	v_pk_mul_f32 v[62:63], v[40:41], v[48:49]
	v_pk_mul_f32 v[138:139], v[126:127], v[134:135]
	v_mov_b32_e32 v127, v140
	v_pk_mul_f32 v[50:51], v[50:51], v[50:51] op_sel:[0,1] op_sel_hi:[1,0]
	v_pk_mul_f32 v[62:63], v[62:63], v[62:63] op_sel:[0,1] op_sel_hi:[1,0]
	v_mov_b32_e32 v136, v130
	v_permlane32_swap_b32_e32 v140, v127
	v_mov_b32_e32 v126, v180
	v_mov_b32_e32 v63, v50
	v_permlane32_swap_b32_e32 v130, v136
	v_permlane32_swap_b32_e32 v180, v126
	v_mov_b32_e32 v181, v140
	v_mov_b32_e32 v51, v62
	v_permlane32_swap_b32_e32 v50, v63
	v_pk_mul_f32 v[130:131], v[130:131], v[136:137]
	v_pk_mul_f32 v[140:141], v[180:181], v[126:127]
	v_permlane32_swap_b32_e32 v62, v51
	s_mov_b64 vcc, 0
